# final RMSNorm row loop: loop-top vmcnt(3)/vmcnt(0) (drained the previous row's four output stores every row) moved to the preheader
# baseline (speedup 1.0000x reference)
.LBB0_1706:
	v_readlane_b32 s8, v252, 8
	v_readlane_b32 s14, v252, 14
	v_readlane_b32 s9, v252, 9
	v_readlane_b32 s10, v252, 10
	v_readlane_b32 s11, v252, 11
	v_readlane_b32 s12, v252, 12
	v_readlane_b32 s13, v252, 13
	v_readlane_b32 s15, v252, 15
	s_cmp_lt_i32 s14, 57
	s_cbranch_scc0 .LBB0_1711
	s_cmp_lt_i32 s15, 57
	s_cbranch_scc1 .LBB0_1711
	v_readlane_b32 s0, v252, 4
	s_lshl_b32 s0, s0, 3
	v_readlane_b32 s1, v252, 16
	s_add_i32 s2, s0, s1
	s_cmpk_gt_i32 s2, 0x7fff
	s_cbranch_scc1 .LBB0_1711
	v_readlane_b32 s5, v252, 2
	s_lshl_b32 s4, s5, 3
	s_add_u32 s0, s12, 0x26d00000
	s_addc_u32 s1, s13, 0
	s_add_i32 s3, s2, s4
	s_cmp_lt_i32 s3, 0x8000
	s_cselect_b32 s6, s3, s2
	s_ashr_i32 s7, s6, 31
	s_lshl_b64 s[6:7], s[6:7], 11
	s_add_u32 s6, s0, s6
	s_waitcnt vmcnt(0)
	v_lshlrev_b32_e32 v18, 4, v225
	v_lshlrev_b32_e32 v16, 3, v225
	s_addc_u32 s7, s1, s7
	s_ashr_i32 s3, s2, 31
	global_load_dwordx4 v[0:3], v18, s[8:9]
	global_load_dwordx4 v[4:7], v18, s[8:9] offset:1024
	global_load_dwordx4 v[8:11], v18, s[8:9] offset:2048
	global_load_dwordx4 v[12:15], v18, s[8:9] offset:3072
	global_load_dwordx2 v[20:21], v16, s[6:7] offset:1536
	global_load_dwordx2 v[22:23], v16, s[6:7] offset:1024
	global_load_dwordx2 v[24:25], v16, s[6:7] offset:512
	global_load_dwordx2 v[30:31], v16, s[6:7]
	s_lshl_b64 s[6:7], s[2:3], 11
	s_add_u32 s6, s0, s6
	s_addc_u32 s7, s1, s7
	global_load_dwordx2 v[36:37], v16, s[6:7] offset:1536
	global_load_dwordx2 v[32:33], v16, s[6:7] offset:1024
	global_load_dwordx2 v[34:35], v16, s[6:7] offset:512
	global_load_dwordx2 v[38:39], v16, s[6:7]
	v_and_b32_e32 v26, 64, v225
	v_add_u32_e32 v26, 64, v26
	v_xor_b32_e32 v27, 1, v225
	v_cmp_lt_i32_e32 vcc, v27, v26
	v_mov_b32_e32 v19, 0
	v_mov_b32_e32 v17, v19
	v_cndmask_b32_e32 v27, v225, v27, vcc
	v_lshlrev_b32_e32 v40, 2, v27
	v_xor_b32_e32 v27, 2, v225
	v_cmp_lt_i32_e32 vcc, v27, v26
	v_lshl_add_u64 v[16:17], s[0:1], 0, v[16:17]
	v_lshl_add_u64 v[18:19], s[10:11], 0, v[18:19]
	v_cndmask_b32_e32 v27, v225, v27, vcc
	v_lshlrev_b32_e32 v41, 2, v27
	v_xor_b32_e32 v27, 4, v225
	v_cmp_lt_i32_e32 vcc, v27, v26
	s_lshl_b32 s5, s5, 4
	v_mov_b32_e32 v46, 0x358637bd
	v_cndmask_b32_e32 v27, v225, v27, vcc
	v_lshlrev_b32_e32 v42, 2, v27
	v_xor_b32_e32 v27, 8, v225
	v_cmp_lt_i32_e32 vcc, v27, v26
	s_mov_b32 s6, 0xf800000
	v_mov_b32_e32 v47, 0x260
	v_cndmask_b32_e32 v27, v225, v27, vcc
	v_lshlrev_b32_e32 v43, 2, v27
	v_xor_b32_e32 v27, 16, v225
	v_cmp_lt_i32_e32 vcc, v27, v26
	s_nop 1
	v_cndmask_b32_e32 v27, v225, v27, vcc
	v_lshlrev_b32_e32 v44, 2, v27
	v_xor_b32_e32 v27, 32, v225
	v_cmp_lt_i32_e32 vcc, v27, v26
	s_nop 1
	v_cndmask_b32_e32 v26, v225, v27, vcc
	v_lshlrev_b32_e32 v45, 2, v26
	s_waitcnt vmcnt(0)
.LBB0_1710:
	s_add_i32 s0, s2, s5
	v_lshlrev_b32_e32 v49, 16, v36
	v_and_b32_e32 v51, 0xffff0000, v38
	v_and_b32_e32 v53, 0xffff0000, v39
	s_cmp_lt_i32 s0, 0x8000
	v_and_b32_e32 v29, 0xffff0000, v36
	v_lshlrev_b32_e32 v26, 16, v37
	v_and_b32_e32 v27, 0xffff0000, v37
	v_lshlrev_b32_e32 v50, 16, v38
	v_lshlrev_b32_e32 v52, 16, v39
	v_lshlrev_b32_e32 v55, 16, v35
	v_lshlrev_b32_e32 v54, 16, v34
	v_and_b32_e32 v57, 0xffff0000, v35
	v_and_b32_e32 v56, 0xffff0000, v34
	v_and_b32_e32 v61, 0xffff0000, v33
	v_mov_b64_e32 v[36:37], v[20:21]
	v_mov_b64_e32 v[34:35], v[24:25]
	v_mul_f32_e32 v20, v53, v53
	v_mul_f32_e32 v24, v51, v51
	v_mov_b32_e32 v21, v49
	s_cselect_b32 s8, s0, s2
	v_lshlrev_b32_e32 v58, 16, v32
	v_and_b32_e32 v59, 0xffff0000, v32
	v_lshlrev_b32_e32 v60, 16, v33
	v_mov_b64_e32 v[32:33], v[22:23]
	v_pk_mul_f32 v[22:23], v[56:57], v[56:57]
	v_mul_f32_e32 v48, v61, v61
	v_pk_fma_f32 v[64:65], v[52:53], v[52:53], v[20:21] op_sel_hi:[1,1,0]
	v_pk_fma_f32 v[24:25], v[50:51], v[50:51], v[24:25] op_sel_hi:[1,1,0]
	s_ashr_i32 s3, s2, 31
	s_ashr_i32 s9, s8, 31
	v_mov_b64_e32 v[38:39], v[30:31]
	v_mul_f32_e32 v30, v59, v59
	v_mov_b32_e32 v62, v54
	v_mov_b32_e32 v63, v56
	v_mov_b32_e32 v56, v55
	v_pk_fma_f32 v[22:23], v[54:55], v[54:55], v[22:23]
	v_pk_fma_f32 v[54:55], v[60:61], v[60:61], v[48:49] op_sel_hi:[1,1,0]
	v_mov_b32_e32 v48, v24
	v_mov_b32_e32 v20, v64
	s_lshl_b64 s[10:11], s[2:3], 12
	s_sub_i32 s2, s0, s4
	s_lshl_b64 s[0:1], s[8:9], 11
	v_mul_f32_e32 v66, v29, v29
	v_mul_f32_e32 v67, v26, v26
	v_mul_f32_e32 v68, v27, v27
	v_mov_b32_e32 v28, v49
	v_pk_fma_f32 v[30:31], v[58:59], v[58:59], v[30:31] op_sel_hi:[1,1,0]
	v_pk_add_f32 v[22:23], v[22:23], v[22:23] op_sel:[0,1] op_sel_hi:[1,0]
	v_pk_mul_f32 v[20:21], v[48:49], v[20:21]
	v_lshl_add_u64 v[48:49], v[16:17], 0, s[0:1]
	v_pk_add_f32 v[24:25], v[24:25], v[64:65]
	v_mov_b32_e32 v31, v67
	v_mov_b32_e32 v55, v68
	v_mov_b32_e32 v23, v66
	global_load_dwordx2 v[64:65], v[48:49], off
	global_load_dwordx2 v[66:67], v[48:49], off offset:512
	global_load_dwordx2 v[68:69], v[48:49], off offset:1024
	global_load_dwordx2 v[70:71], v[48:49], off offset:1536
	v_mov_b32_e32 v25, v21
	v_pk_add_f32 v[30:31], v[30:31], v[54:55]
	v_pk_add_f32 v[20:21], v[24:25], v[22:23]
	v_lshl_add_u64 v[54:55], v[18:19], 0, s[10:11]
	v_pk_add_f32 v[20:21], v[20:21], v[30:31]
	s_cmp_lt_i32 s2, 0x8000
	v_add_f32_e32 v20, v20, v21
	ds_bpermute_b32 v21, v40, v20
	s_waitcnt lgkmcnt(0)
	v_add_f32_e32 v20, v20, v21
	ds_bpermute_b32 v21, v41, v20
	s_waitcnt lgkmcnt(0)
	v_add_f32_e32 v20, v20, v21
	ds_bpermute_b32 v21, v42, v20
	s_waitcnt lgkmcnt(0)
	v_add_f32_e32 v20, v20, v21
	ds_bpermute_b32 v21, v43, v20
	s_waitcnt lgkmcnt(0)
	v_add_f32_e32 v20, v20, v21
	ds_bpermute_b32 v21, v44, v20
	s_waitcnt lgkmcnt(0)
	v_add_f32_e32 v20, v20, v21
	ds_bpermute_b32 v21, v45, v20
	s_waitcnt lgkmcnt(0)
	v_add_f32_e32 v20, v20, v21
	v_fmamk_f32 v20, v20, 0x3a800000, v46
	v_mul_f32_e32 v21, 0x4f800000, v20
	v_cmp_gt_f32_e32 vcc, s6, v20
	s_nop 1
	v_cndmask_b32_e32 v20, v20, v21, vcc
	v_sqrt_f32_e32 v21, v20
	s_nop 0
	v_add_u32_e32 v22, -1, v21
	v_add_u32_e32 v23, 1, v21
	v_fma_f32 v24, -v22, v21, v20
	v_fma_f32 v25, -v23, v21, v20
	v_cmp_ge_f32_e64 s[0:1], 0, v24
	s_nop 1
	v_cndmask_b32_e64 v21, v21, v22, s[0:1]
	v_cmp_lt_f32_e64 s[0:1], 0, v25
	s_nop 1
	v_cndmask_b32_e64 v21, v21, v23, s[0:1]
	v_mul_f32_e32 v22, 0x37800000, v21
	v_cndmask_b32_e32 v21, v21, v22, vcc
	v_cmp_class_f32_e32 vcc, v20, v47
	s_nop 1
	v_cndmask_b32_e32 v20, v21, v20, vcc
	v_div_scale_f32 v21, s[0:1], v20, v20, 1.0
	v_rcp_f32_e32 v23, v21
	v_div_scale_f32 v22, vcc, 1.0, v20, 1.0
	v_fma_f32 v24, -v21, v23, 1.0
	v_fmac_f32_e32 v23, v24, v23
	v_mul_f32_e32 v24, v22, v23
	v_fma_f32 v25, -v21, v24, v22
	v_fmac_f32_e32 v24, v25, v23
	v_fma_f32 v21, -v21, v24, v22
	v_div_fmas_f32 v21, v21, v23, v24
	v_div_fixup_f32 v20, v21, v20, 1.0
	v_pk_mul_f32 v[24:25], v[20:21], v[50:51] op_sel_hi:[0,1]
	v_pk_mul_f32 v[22:23], v[20:21], v[52:53] op_sel_hi:[0,1]
	v_pk_mul_f32 v[30:31], v[20:21], v[62:63] op_sel_hi:[0,1]
	v_pk_mul_f32 v[52:53], v[20:21], v[60:61] op_sel_hi:[0,1]
	v_pk_mul_f32 v[48:49], v[20:21], v[56:57] op_sel_hi:[0,1]
	v_pk_mul_f32 v[50:51], v[20:21], v[58:59] op_sel_hi:[0,1]
	v_pk_mul_f32 v[56:57], v[20:21], v[28:29] op_sel_hi:[0,1]
	v_pk_mul_f32 v[58:59], v[20:21], v[26:27] op_sel_hi:[0,1]
	v_pk_mul_f32 v[22:23], v[22:23], v[2:3]
	v_pk_mul_f32 v[20:21], v[24:25], v[0:1]
	v_pk_mul_f32 v[24:25], v[30:31], v[4:5]
	v_pk_mul_f32 v[30:31], v[52:53], v[10:11]
	v_pk_mul_f32 v[26:27], v[48:49], v[6:7]
	v_pk_mul_f32 v[28:29], v[50:51], v[8:9]
	v_pk_mul_f32 v[50:51], v[58:59], v[14:15]
	v_pk_mul_f32 v[48:49], v[56:57], v[12:13]
	global_store_dwordx4 v[54:55], v[20:23], off
	global_store_dwordx4 v[54:55], v[24:27], off offset:1024
	global_store_dwordx4 v[54:55], v[28:31], off offset:2048
	global_store_dwordx4 v[54:55], v[48:51], off offset:3072
	s_waitcnt vmcnt(4)
	v_mov_b64_e32 v[20:21], v[70:71]
	v_mov_b64_e32 v[22:23], v[68:69]
	v_mov_b64_e32 v[24:25], v[66:67]
	v_mov_b64_e32 v[30:31], v[64:65]
	s_cbranch_scc1 .LBB0_1710
